# baseline (speedup 1.0000x reference)
.LBB1_36:
	s_or_b64 exec, exec, s[2:3]
	s_mul_i32 s2, s24, 0x500
	v_or_b32_e32 v68, s2, v101
	v_mov_b32_e32 v69, 0
	s_add_i32 s3, s2, 0x100
	v_lshl_add_u64 v[66:67], v[68:69], 2, s[6:7]
	v_or_b32_e32 v64, s3, v101
	v_mov_b32_e32 v65, v69
	s_add_i32 s3, s2, 0x140
	global_load_dword v103, v[66:67], off
	global_load_dword v108, v[66:67], off offset:256
	global_load_dword v109, v[66:67], off offset:512
	global_load_dword v110, v[66:67], off offset:768
	v_lshl_add_u64 v[72:73], v[64:65], 2, s[6:7]
	v_or_b32_e32 v64, s3, v101
	s_add_i32 s3, s2, 0x180
	global_load_dword v111, v[72:73], off
	v_lshl_add_u64 v[64:65], v[64:65], 2, s[6:7]
	v_or_b32_e32 v70, s3, v101
	v_mov_b32_e32 v71, v69
	global_load_dword v112, v[64:65], off
	v_lshl_add_u64 v[70:71], v[70:71], 2, s[6:7]
	global_load_dword v113, v[70:71], off
	s_add_i32 s3, s2, 0x1c0
	v_mov_b32_e32 v75, v69
	s_add_i32 s4, s2, 0x200
	s_add_i32 s5, s2, 0x240
	s_add_i32 s11, s2, 0x280
	v_or_b32_e32 v74, s3, v101
	v_mov_b32_e32 v77, v69
	v_mov_b32_e32 v79, v69
	v_mov_b32_e32 v81, v69
	v_or_b32_e32 v76, s4, v101
	v_or_b32_e32 v78, s5, v101
	v_or_b32_e32 v80, s11, v101
	v_lshl_add_u64 v[90:91], v[74:75], 2, s[6:7]
	v_lshl_add_u64 v[88:89], v[76:77], 2, s[6:7]
	v_lshl_add_u64 v[82:83], v[78:79], 2, s[6:7]
	v_lshl_add_u64 v[80:81], v[80:81], 2, s[6:7]
	global_load_dword v114, v[90:91], off
	global_load_dword v115, v[88:89], off
	global_load_dword v116, v[82:83], off
	global_load_dword v117, v[80:81], off
	s_add_i32 s15, s2, 0x300
	s_add_i32 s3, s2, 0x3c0
	v_mov_b32_e32 v87, v69
	v_or_b32_e32 v86, s15, v101
	v_or_b32_e32 v74, s3, v101
	v_lshl_add_u64 v[96:97], v[86:87], 2, s[6:7]
	v_lshl_add_u64 v[86:87], v[74:75], 2, s[6:7]
	s_add_i32 s16, s2, 0x340
	s_add_i32 s17, s2, 0x380
	v_mov_b32_e32 v93, v69
	v_mov_b32_e32 v105, v69
	v_or_b32_e32 v92, s16, v101
	v_or_b32_e32 v104, s17, v101
	v_lshl_add_u64 v[94:95], v[92:93], 2, s[6:7]
	v_lshl_add_u64 v[92:93], v[104:105], 2, s[6:7]
	s_add_i32 s14, s2, 0x2c0
	v_mov_b32_e32 v85, v69
	s_add_i32 s4, s2, 0x400
	v_or_b32_e32 v84, s14, v101
	s_add_i32 s5, s2, 0x440
	s_add_i32 s11, s2, 0x480
	v_or_b32_e32 v76, s4, v101
	v_lshl_add_u64 v[98:99], v[84:85], 2, s[6:7]
	v_mov_b32_e32 v107, v69
	v_or_b32_e32 v78, s5, v101
	v_or_b32_e32 v106, s11, v101
	v_lshl_add_u64 v[84:85], v[76:77], 2, s[6:7]
	global_load_dword v118, v[98:99], off
	global_load_dword v119, v[96:97], off
	global_load_dword v120, v[94:95], off
	global_load_dword v121, v[92:93], off
	global_load_dword v122, v[86:87], off
	v_lshl_add_u64 v[78:79], v[78:79], 2, s[6:7]
	v_lshl_add_u64 v[76:77], v[106:107], 2, s[6:7]
	s_addk_i32 s2, 0x4c0
	s_mov_b32 s14, 0xf800000
	s_mov_b32 s11, 0x41e6d4ca
	s_waitcnt vmcnt(15)
	v_add_f32_e32 v74, 0, v103
	s_waitcnt vmcnt(14)
	v_add_f32_e32 v74, v74, v108
	s_waitcnt vmcnt(13)
	v_add_f32_e32 v74, v74, v109
	s_waitcnt vmcnt(12)
	v_add_f32_e32 v74, v74, v110
	global_load_dword v103, v[84:85], off
	global_load_dword v109, v[76:77], off
	s_waitcnt vmcnt(13)
	v_add_f32_e32 v74, v74, v111
	s_waitcnt vmcnt(12)
	v_add_f32_e32 v74, v74, v112
	global_load_dword v112, v[66:67], off offset:64
	s_waitcnt vmcnt(12)
	v_add_f32_e32 v104, v74, v113
	v_or_b32_e32 v74, s2, v101
	v_lshl_add_u64 v[74:75], v[74:75], 2, s[6:7]
	global_load_dword v110, v[74:75], off
	s_waitcnt vmcnt(12)
	v_add_f32_e32 v104, v104, v114
	s_waitcnt vmcnt(11)
	v_add_f32_e32 v104, v104, v115
	s_waitcnt vmcnt(10)
	v_add_f32_e32 v104, v104, v116
	s_waitcnt vmcnt(9)
	v_add_f32_e32 v111, v104, v117
	v_or_b32_e32 v104, 16, v68
	v_lshl_add_u64 v[106:107], v[104:105], 2, s[6:7]
	global_load_dword v113, v[106:107], off offset:256
	global_load_dword v108, v[78:79], off
	s_waitcnt vmcnt(10)
	v_add_f32_e32 v104, v111, v118
	s_waitcnt vmcnt(9)
	v_add_f32_e32 v104, v104, v119
	s_waitcnt vmcnt(8)
	v_add_f32_e32 v104, v104, v120
	s_waitcnt vmcnt(7)
	v_add_f32_e32 v104, v104, v121
	s_waitcnt vmcnt(6)
	v_add_f32_e32 v104, v104, v122
	s_waitcnt vmcnt(5)
	v_add_f32_e32 v103, v104, v103
	s_waitcnt vmcnt(3)
	v_add_f32_e32 v112, 0, v112
	s_waitcnt vmcnt(1)
	v_add_f32_e32 v112, v112, v113
	s_waitcnt vmcnt(0)
	v_add_f32_e32 v103, v103, v108
	v_add_f32_e32 v103, v103, v109
	v_add_f32_e32 v103, v103, v110
	v_cmp_gt_f32_e32 vcc, s14, v103
	v_mul_f32_e32 v104, 0x4f800000, v103
	s_nop 0
	v_cndmask_b32_e32 v104, v103, v104, vcc
	v_sqrt_f32_e32 v103, v104
	s_nop 0
	v_add_u32_e32 v105, -1, v103
	v_fma_f32 v108, -v105, v103, v104
	v_cmp_ge_f32_e64 s[2:3], 0, v108
	v_add_u32_e32 v108, 1, v103
	s_nop 0
	v_cndmask_b32_e64 v105, v103, v105, s[2:3]
	v_fma_f32 v103, -v108, v103, v104
	v_cmp_lt_f32_e64 s[2:3], 0, v103
	s_nop 1
	v_cndmask_b32_e64 v103, v105, v108, s[2:3]
	v_mul_f32_e32 v105, 0x37800000, v103
	v_cndmask_b32_e32 v105, v103, v105, vcc
	v_mov_b32_e32 v103, 0x260
	v_cmp_class_f32_e32 vcc, v104, v103
	s_nop 1
	v_cndmask_b32_e32 v104, v105, v104, vcc
	v_add_f32_e32 v104, 0x322bcc77, v104
	v_div_scale_f32 v108, s[2:3], v104, v104, s11
	v_rcp_f32_e32 v105, v108
	s_nop 0
	v_fma_f32 v109, -v108, v105, 1.0
	v_fmac_f32_e32 v105, v109, v105
	global_load_dword v109, v[106:107], off offset:512
	s_nop 0
	global_load_dword v106, v[106:107], off offset:768
	s_nop 0
	global_load_dword v107, v[72:73], off offset:64
	global_load_dword v110, v[64:65], off offset:64
	global_load_dword v111, v[70:71], off offset:64
	global_load_dword v114, v[90:91], off offset:64
	global_load_dword v115, v[88:89], off offset:64
	global_load_dword v116, v[82:83], off offset:64
	global_load_dword v113, v[80:81], off offset:64
	s_waitcnt vmcnt(8)
	v_add_f32_e32 v109, v112, v109
	s_waitcnt vmcnt(7)
	v_add_f32_e32 v106, v109, v106
	s_waitcnt vmcnt(6)
	v_add_f32_e32 v106, v106, v107
	global_load_dword v107, v[98:99], off offset:64
	global_load_dword v109, v[96:97], off offset:64
	s_waitcnt vmcnt(7)
	v_add_f32_e32 v106, v106, v110
	s_waitcnt vmcnt(6)
	v_add_f32_e32 v106, v106, v111
	s_waitcnt vmcnt(5)
	v_add_f32_e32 v106, v106, v114
	s_waitcnt vmcnt(4)
	v_add_f32_e32 v106, v106, v115
	s_waitcnt vmcnt(3)
	v_add_f32_e32 v106, v106, v116
	s_waitcnt vmcnt(2)
	v_add_f32_e32 v106, v106, v113
	global_load_dword v110, v[94:95], off offset:64
	global_load_dword v111, v[92:93], off offset:64
	global_load_dword v112, v[86:87], off offset:64
	global_load_dword v113, v[84:85], off offset:64
	global_load_dword v114, v[78:79], off offset:64
	global_load_dword v115, v[76:77], off offset:64
	global_load_dword v116, v[74:75], off offset:64
	s_waitcnt vmcnt(8)
	v_add_f32_e32 v106, v106, v107
	s_waitcnt vmcnt(7)
	v_add_f32_e32 v109, v106, v109
	s_waitcnt vmcnt(6)
	v_add_f32_e32 v109, v109, v110
	s_waitcnt vmcnt(5)
	v_add_f32_e32 v109, v109, v111
	s_waitcnt vmcnt(4)
	v_add_f32_e32 v109, v109, v112
	s_waitcnt vmcnt(3)
	v_add_f32_e32 v109, v109, v113
	s_waitcnt vmcnt(2)
	v_add_f32_e32 v109, v109, v114
	s_waitcnt vmcnt(1)
	v_add_f32_e32 v109, v109, v115
	s_waitcnt vmcnt(0)
	v_add_f32_e32 v109, v109, v116
	v_cmp_gt_f32_e64 s[2:3], s14, v109
	v_mul_f32_e32 v110, 0x4f800000, v109
	v_div_scale_f32 v107, vcc, s11, v104, s11
	v_cndmask_b32_e64 v109, v109, v110, s[2:3]
	v_sqrt_f32_e32 v110, v109
	v_mul_f32_e32 v106, v107, v105
	v_fma_f32 v111, -v108, v106, v107
	v_fmac_f32_e32 v106, v111, v105
	v_fma_f32 v107, -v108, v106, v107
	v_add_u32_e32 v108, -1, v110
	v_fma_f32 v111, -v108, v110, v109
	v_cmp_ge_f32_e64 s[4:5], 0, v111
	v_add_u32_e32 v111, 1, v110
	s_nop 0
	v_cndmask_b32_e64 v108, v110, v108, s[4:5]
	v_fma_f32 v110, -v111, v110, v109
	v_cmp_lt_f32_e64 s[4:5], 0, v110
	s_nop 1
	v_cndmask_b32_e64 v108, v108, v111, s[4:5]
	v_mul_f32_e32 v110, 0x37800000, v108
	v_cndmask_b32_e64 v108, v108, v110, s[2:3]
	v_cmp_class_f32_e64 s[2:3], v109, v103
	v_or_b32_e32 v110, 32, v68
	v_mov_b32_e32 v111, v69
	v_cndmask_b32_e64 v108, v108, v109, s[2:3]
	global_load_dword v109, v[66:67], off offset:128
	v_lshl_add_u64 v[112:113], v[110:111], 2, s[6:7]
	global_load_dword v110, v[112:113], off offset:256
	global_load_dword v111, v[112:113], off offset:512
	s_nop 0
	global_load_dword v112, v[112:113], off offset:768
	s_nop 0
	global_load_dword v113, v[72:73], off offset:128
	global_load_dword v114, v[66:67], off offset:192
	v_or_b32_e32 v68, 48, v68
	v_lshl_add_u64 v[66:67], v[68:69], 2, s[6:7]
	global_load_dword v68, v[66:67], off offset:256
	global_load_dword v115, v[66:67], off offset:512
	s_nop 0
	global_load_dword v66, v[66:67], off offset:768
	s_nop 0
	global_load_dword v67, v[64:65], off offset:128
	s_nop 0
	global_load_dword v72, v[72:73], off offset:192
	s_nop 0
	global_load_dword v73, v[70:71], off offset:128
	global_load_dword v116, v[64:65], off offset:192
	s_nop 0
	global_load_dword v65, v[90:91], off offset:128
	s_nop 0
	global_load_dword v70, v[70:71], off offset:192
	s_nop 0
	global_load_dword v71, v[88:89], off offset:128
	s_nop 0
	global_load_dword v90, v[90:91], off offset:192
	s_nop 0
	global_load_dword v91, v[82:83], off offset:128
	s_nop 0
	global_load_dword v88, v[88:89], off offset:192
	s_nop 0
	global_load_dword v89, v[80:81], off offset:128
	s_nop 0
	global_load_dword v82, v[82:83], off offset:192
	s_nop 0
	global_load_dword v83, v[98:99], off offset:128
	s_nop 0
	global_load_dword v80, v[80:81], off offset:192
	s_nop 0
	global_load_dword v81, v[96:97], off offset:128
	s_nop 0
	global_load_dword v98, v[98:99], off offset:192
	s_nop 0
	global_load_dword v99, v[94:95], off offset:128
	s_nop 0
	global_load_dword v96, v[96:97], off offset:192
	s_nop 0
	global_load_dword v97, v[92:93], off offset:128
	s_nop 0
	global_load_dword v94, v[94:95], off offset:192
	s_nop 0
	global_load_dword v95, v[86:87], off offset:128
	s_nop 0
	global_load_dword v92, v[92:93], off offset:192
	s_nop 0
	global_load_dword v93, v[84:85], off offset:128
	s_nop 0
	global_load_dword v86, v[86:87], off offset:192
	s_nop 0
	global_load_dword v87, v[78:79], off offset:128
	s_nop 0
	global_load_dword v84, v[84:85], off offset:192
	s_nop 0
	global_load_dword v85, v[76:77], off offset:128
	s_nop 0
	global_load_dword v78, v[78:79], off offset:192
	s_nop 0
	global_load_dword v79, v[74:75], off offset:128
	v_div_fmas_f32 v64, v107, v105, v106
	global_load_dword v76, v[76:77], off offset:192
	s_mul_i32 s2, s23, 0x1f80
	global_load_dword v74, v[74:75], off offset:192
	v_add_f32_e32 v108, 0x322bcc77, v108
	s_add_i32 s6, s8, s2
	v_div_scale_f32 v77, s[2:3], v108, v108, s11
	v_rcp_f32_e32 v117, v77
	v_div_fixup_f32 v64, v64, v104, s11
	v_lshrrev_b32_e32 v75, 4, v100
	v_fma_f32 v104, -v77, v117, 1.0
	v_fmac_f32_e32 v117, v104, v117
	v_div_scale_f32 v104, vcc, s11, v108, s11
	v_mul_f32_e32 v105, v104, v117
	s_waitcnt vmcnt(39)
	v_add_f32_e32 v106, 0, v109
	s_waitcnt vmcnt(38)
	v_add_f32_e32 v106, v106, v110
	s_waitcnt vmcnt(37)
	v_add_f32_e32 v106, v106, v111
	s_waitcnt vmcnt(36)
	v_add_f32_e32 v106, v106, v112
	s_waitcnt vmcnt(35)
	v_add_f32_e32 v106, v106, v113
	s_waitcnt vmcnt(30)
	v_add_f32_e32 v67, v106, v67
	s_waitcnt vmcnt(28)
	v_add_f32_e32 v67, v67, v73
	s_waitcnt vmcnt(26)
	v_add_f32_e32 v65, v67, v65
	s_waitcnt vmcnt(24)
	v_add_f32_e32 v65, v65, v71
	s_waitcnt vmcnt(22)
	v_add_f32_e32 v65, v65, v91
	s_waitcnt vmcnt(20)
	v_add_f32_e32 v65, v65, v89
	s_waitcnt vmcnt(18)
	v_add_f32_e32 v65, v65, v83
	s_waitcnt vmcnt(16)
	v_add_f32_e32 v65, v65, v81
	s_waitcnt vmcnt(14)
	v_add_f32_e32 v65, v65, v99
	s_waitcnt vmcnt(12)
	v_add_f32_e32 v65, v65, v97
	s_waitcnt vmcnt(10)
	v_add_f32_e32 v65, v65, v95
	s_waitcnt vmcnt(8)
	v_add_f32_e32 v65, v65, v93
	s_waitcnt vmcnt(6)
	v_add_f32_e32 v65, v65, v87
	s_waitcnt vmcnt(4)
	v_add_f32_e32 v65, v65, v85
	s_waitcnt vmcnt(2)
	v_add_f32_e32 v65, v65, v79
	v_cmp_gt_f32_e64 s[2:3], s14, v65
	v_mul_f32_e32 v67, 0x4f800000, v65
	v_add_f32_e32 v81, 0, v114
	v_cndmask_b32_e64 v65, v65, v67, s[2:3]
	v_add_f32_e32 v68, v81, v68
	v_sqrt_f32_e32 v67, v65
	v_add_f32_e32 v68, v68, v115
	v_add_f32_e32 v66, v68, v66
	v_add_f32_e32 v66, v66, v72
	v_fma_f32 v71, -v77, v105, v104
	v_add_f32_e32 v66, v66, v116
	v_fmac_f32_e32 v105, v71, v117
	v_add_u32_e32 v73, -1, v67
	v_add_f32_e32 v66, v66, v70
	v_fma_f32 v71, -v77, v105, v104
	v_fma_f32 v77, -v73, v67, v65
	v_add_f32_e32 v66, v66, v90
	v_cmp_ge_f32_e64 s[4:5], 0, v77
	v_add_u32_e32 v77, 1, v67
	v_add_f32_e32 v66, v66, v88
	v_cndmask_b32_e64 v73, v67, v73, s[4:5]
	v_fma_f32 v67, -v77, v67, v65
	v_add_f32_e32 v66, v66, v82
	v_cmp_lt_f32_e64 s[4:5], 0, v67
	v_add_f32_e32 v66, v66, v80
	v_add_f32_e32 v66, v66, v98
	v_cndmask_b32_e64 v67, v73, v77, s[4:5]
	v_mul_f32_e32 v73, 0x37800000, v67
	v_add_f32_e32 v66, v66, v96
	v_cndmask_b32_e64 v67, v67, v73, s[2:3]
	v_cmp_class_f32_e64 s[2:3], v65, v103
	v_add_f32_e32 v66, v66, v94
	v_add_f32_e32 v66, v66, v92
	v_cndmask_b32_e64 v65, v67, v65, s[2:3]
	v_add_f32_e32 v67, 0x322bcc77, v65
	v_add_f32_e32 v66, v66, v86
	v_div_scale_f32 v73, s[2:3], v67, v67, s11
	v_add_f32_e32 v66, v66, v84
	v_rcp_f32_e32 v77, v73
	v_add_f32_e32 v66, v66, v78
	s_waitcnt vmcnt(1)
	v_add_f32_e32 v66, v66, v76
	s_waitcnt vmcnt(0)
	v_add_f32_e32 v66, v66, v74
	v_cmp_gt_f32_e64 s[2:3], s14, v66
	v_mul_f32_e32 v68, 0x4f800000, v66
	v_div_fmas_f32 v65, v71, v117, v105
	v_fma_f32 v71, -v73, v77, 1.0
	v_cndmask_b32_e64 v66, v66, v68, s[2:3]
	v_fmac_f32_e32 v77, v71, v77
	v_div_scale_f32 v71, vcc, s11, v67, s11
	v_sqrt_f32_e32 v68, v66
	v_mul_f32_e32 v79, v71, v77
	v_fma_f32 v70, -v73, v79, v71
	v_fmac_f32_e32 v79, v70, v77
	v_fma_f32 v70, -v73, v79, v71
	v_add_u32_e32 v71, -1, v68
	v_fma_f32 v72, -v71, v68, v66
	v_cmp_ge_f32_e64 s[4:5], 0, v72
	v_add_u32_e32 v72, 1, v68
	v_div_fixup_f32 v65, v65, v108, s11
	v_cndmask_b32_e64 v71, v68, v71, s[4:5]
	v_fma_f32 v68, -v72, v68, v66
	v_cmp_lt_f32_e64 s[4:5], 0, v68
	s_nop 1
	v_cndmask_b32_e64 v68, v71, v72, s[4:5]
	v_mul_f32_e32 v71, 0x37800000, v68
	v_cndmask_b32_e64 v68, v68, v71, s[2:3]
	v_cmp_class_f32_e64 s[2:3], v66, v103
	s_nop 1
	v_cndmask_b32_e64 v66, v68, v66, s[2:3]
	v_add_f32_e32 v72, 0x322bcc77, v66
	v_div_scale_f32 v66, s[2:3], v72, v72, s11
	v_rcp_f32_e32 v73, v66
	v_div_fmas_f32 v68, v70, v77, v79
	v_div_fixup_f32 v68, v68, v67, s11
	s_movk_i32 s2, 0x88
	v_fma_f32 v67, -v66, v73, 1.0
	v_fmac_f32_e32 v73, v67, v73
	v_div_scale_f32 v67, vcc, s11, v72, s11
	v_mul_f32_e32 v70, v67, v73
	v_fma_f32 v71, -v66, v70, v67
	v_fmac_f32_e32 v70, v71, v73
	v_fma_f32 v67, -v66, v70, v67
	v_and_b32_e32 v66, 0x70, v100
	v_add_u32_e32 v71, s10, v66
	ds_read_b128 v[76:79], v71 offset:8832
	v_div_fmas_f32 v67, v67, v73, v70
	v_div_fixup_f32 v70, v67, v72, s11
	v_lshlrev_b32_e32 v67, 3, v75
	v_add_u32_e32 v72, s6, v67
	s_waitcnt lgkmcnt(0)
	v_mul_f32_e32 v73, v76, v64
	v_fmaak_f32 v60, v60, v73, 0xc1e6d4ca
	v_exp_f32_e32 v73, v60
	v_mul_f32_e32 v60, v77, v64
	v_fmaak_f32 v60, v61, v60, 0xc1e6d4ca
	v_mul_f32_e32 v61, v78, v64
	v_fmaak_f32 v61, v62, v61, 0xc1e6d4ca
	v_mul_f32_e32 v62, v79, v64
	v_fmaak_f32 v62, v63, v62, 0xc1e6d4ca
	v_exp_f32_e32 v61, v61
	v_exp_f32_e32 v62, v62
	v_exp_f32_e32 v74, v60
	v_mad_u32_u24 v60, v101, s2, v72
	s_mov_b32 s10, s9
	v_cvt_pk_bf16_f32 v63, v61, v62
	v_mul_f32_e32 v61, v76, v65
	v_fmaak_f32 v56, v56, v61, 0xc1e6d4ca
	v_mul_f32_e32 v61, v77, v65
	v_fmaak_f32 v57, v57, v61, 0xc1e6d4ca
	v_exp_f32_e32 v61, v57
	v_mul_f32_e32 v57, v78, v65
	v_cvt_pk_bf16_f32 v62, v73, v74
	v_fmaak_f32 v57, v58, v57, 0xc1e6d4ca
	ds_write_b64 v60, v[62:63] offset:10240
	v_exp_f32_e32 v62, v57
	v_mul_f32_e32 v57, v79, v65
	v_fmaak_f32 v57, v59, v57, 0xc1e6d4ca
	v_exp_f32_e32 v56, v56
	v_exp_f32_e32 v59, v57
	v_mov_b32_e32 v57, 0x880
	v_mad_u32_u24 v57, v101, s2, v57
	v_add_u32_e32 v58, v72, v57
	v_cvt_pk_bf16_f32 v63, v62, v59
	v_cvt_pk_bf16_f32 v62, v56, v61
	v_mul_f32_e32 v56, v76, v68
	v_fmaak_f32 v52, v52, v56, 0xc1e6d4ca
	v_exp_f32_e32 v56, v52
	v_mul_f32_e32 v52, v77, v68
	v_fmaak_f32 v52, v53, v52, 0xc1e6d4ca
	v_exp_f32_e32 v59, v52
	v_mul_f32_e32 v52, v78, v68
	v_fmaak_f32 v52, v54, v52, 0xc1e6d4ca
	v_exp_f32_e32 v54, v52
	v_mul_f32_e32 v52, v79, v68
	v_fmaak_f32 v52, v55, v52, 0xc1e6d4ca
	v_exp_f32_e32 v55, v52
	v_mov_b32_e32 v52, 0x1100
	v_mad_u32_u24 v52, v101, s2, v52
	v_add_u32_e32 v53, v72, v52
	v_cvt_pk_bf16_f32 v55, v54, v55
	v_cvt_pk_bf16_f32 v54, v56, v59
	ds_write_b64 v53, v[54:55] offset:10240
	v_mul_f32_e32 v54, v76, v70
	v_fmaak_f32 v48, v48, v54, 0xc1e6d4ca
	v_exp_f32_e32 v54, v48
	v_mul_f32_e32 v48, v77, v70
	v_fmaak_f32 v48, v49, v48, 0xc1e6d4ca
	v_exp_f32_e32 v49, v48
	v_mul_f32_e32 v48, v78, v70
	v_fmaak_f32 v48, v50, v48, 0xc1e6d4ca
	v_exp_f32_e32 v50, v48
	v_mul_f32_e32 v48, v79, v70
	v_fmaak_f32 v48, v51, v48, 0xc1e6d4ca
	v_exp_f32_e32 v51, v48
	v_mov_b32_e32 v48, 0x1980
	v_mad_u32_u24 v56, v101, s2, v48
	v_add_u32_e32 v48, v72, v56
	v_cvt_pk_bf16_f32 v51, v50, v51
	v_cvt_pk_bf16_f32 v50, v54, v49
	ds_write_b64 v58, v[62:63] offset:10240
	ds_write_b64 v48, v[50:51] offset:10240
	ds_read_b128 v[76:79], v71 offset:8896
	s_mov_b32 s11, s9
	s_waitcnt lgkmcnt(0)
	v_mul_f32_e32 v49, v76, v64
	v_fmaak_f32 v44, v44, v49, 0xc1e6d4ca
	v_mul_f32_e32 v49, v78, v64
	v_fmaak_f32 v46, v46, v49, 0xc1e6d4ca
	v_mul_f32_e32 v49, v79, v64
	v_fmaak_f32 v47, v47, v49, 0xc1e6d4ca
	v_exp_f32_e32 v46, v46
	v_exp_f32_e32 v47, v47
	v_mul_f32_e32 v49, v77, v64
	v_fmaak_f32 v45, v45, v49, 0xc1e6d4ca
	v_exp_f32_e32 v49, v45
	v_cvt_pk_bf16_f32 v45, v46, v47
	v_mul_f32_e32 v46, v76, v65
	v_fmaak_f32 v40, v40, v46, 0xc1e6d4ca
	v_mul_f32_e32 v46, v77, v65
	v_fmaak_f32 v41, v41, v46, 0xc1e6d4ca
	v_mul_f32_e32 v46, v78, v65
	v_fmaak_f32 v42, v42, v46, 0xc1e6d4ca
	v_mul_f32_e32 v46, v79, v65
	v_fmaak_f32 v43, v43, v46, 0xc1e6d4ca
	v_exp_f32_e32 v40, v40
	v_exp_f32_e32 v42, v42
	v_exp_f32_e32 v43, v43
	v_exp_f32_e32 v46, v41
	v_exp_f32_e32 v44, v44
	v_cvt_pk_bf16_f32 v41, v42, v43
	v_cvt_pk_bf16_f32 v40, v40, v46
	ds_write_b64 v58, v[40:41] offset:10272
	v_mul_f32_e32 v40, v76, v68
	v_fmaak_f32 v36, v36, v40, 0xc1e6d4ca
	v_mul_f32_e32 v40, v78, v68
	v_fmaak_f32 v38, v38, v40, 0xc1e6d4ca
	v_mul_f32_e32 v40, v79, v68
	v_fmaak_f32 v39, v39, v40, 0xc1e6d4ca
	v_exp_f32_e32 v38, v38
	v_exp_f32_e32 v39, v39
	v_mul_f32_e32 v40, v77, v68
	v_fmaak_f32 v37, v37, v40, 0xc1e6d4ca
	v_exp_f32_e32 v40, v37
	v_cvt_pk_bf16_f32 v37, v38, v39
	v_mul_f32_e32 v38, v76, v70
	v_fmaak_f32 v32, v32, v38, 0xc1e6d4ca
	v_mul_f32_e32 v38, v77, v70
	v_fmaak_f32 v33, v33, v38, 0xc1e6d4ca
	v_mul_f32_e32 v38, v78, v70
	v_fmaak_f32 v34, v34, v38, 0xc1e6d4ca
	v_mul_f32_e32 v38, v79, v70
	v_fmaak_f32 v35, v35, v38, 0xc1e6d4ca
	v_exp_f32_e32 v36, v36
	v_exp_f32_e32 v32, v32
	v_exp_f32_e32 v34, v34
	v_exp_f32_e32 v35, v35
	v_exp_f32_e32 v38, v33
	v_cvt_pk_bf16_f32 v44, v44, v49
	v_cvt_pk_bf16_f32 v36, v36, v40
	v_cvt_pk_bf16_f32 v33, v34, v35
	v_cvt_pk_bf16_f32 v32, v32, v38
	ds_write_b64 v60, v[44:45] offset:10272
	ds_write_b64 v53, v[36:37] offset:10272
	ds_write_b64 v48, v[32:33] offset:10272
	ds_read_b128 v[32:35], v71 offset:8960
	s_waitcnt lgkmcnt(0)
	v_mul_f32_e32 v36, v32, v64
	v_fmaak_f32 v28, v28, v36, 0xc1e6d4ca
	v_mul_f32_e32 v36, v34, v64
	v_fmaak_f32 v30, v30, v36, 0xc1e6d4ca
	v_mul_f32_e32 v36, v35, v64
	v_fmaak_f32 v31, v31, v36, 0xc1e6d4ca
	v_exp_f32_e32 v30, v30
	v_exp_f32_e32 v31, v31
	v_mul_f32_e32 v36, v33, v64
	v_fmaak_f32 v29, v29, v36, 0xc1e6d4ca
	v_exp_f32_e32 v36, v29
	v_cvt_pk_bf16_f32 v29, v30, v31
	v_mul_f32_e32 v30, v32, v65
	v_fmaak_f32 v24, v24, v30, 0xc1e6d4ca
	v_mul_f32_e32 v30, v33, v65
	v_fmaak_f32 v25, v25, v30, 0xc1e6d4ca
	v_mul_f32_e32 v30, v34, v65
	v_fmaak_f32 v26, v26, v30, 0xc1e6d4ca
	v_mul_f32_e32 v30, v35, v65
	v_fmaak_f32 v27, v27, v30, 0xc1e6d4ca
	v_exp_f32_e32 v24, v24
	v_exp_f32_e32 v26, v26
	v_exp_f32_e32 v27, v27
	v_exp_f32_e32 v30, v25
	v_exp_f32_e32 v28, v28
	v_cvt_pk_bf16_f32 v25, v26, v27
	v_cvt_pk_bf16_f32 v24, v24, v30
	ds_write_b64 v58, v[24:25] offset:10304
	v_mul_f32_e32 v24, v32, v68
	v_fmaak_f32 v20, v20, v24, 0xc1e6d4ca
	v_mul_f32_e32 v24, v34, v68
	v_fmaak_f32 v22, v22, v24, 0xc1e6d4ca
	v_mul_f32_e32 v24, v35, v68
	v_fmaak_f32 v23, v23, v24, 0xc1e6d4ca
	v_exp_f32_e32 v22, v22
	v_exp_f32_e32 v23, v23
	v_mul_f32_e32 v24, v33, v68
	v_fmaak_f32 v21, v21, v24, 0xc1e6d4ca
	v_exp_f32_e32 v24, v21
	v_cvt_pk_bf16_f32 v21, v22, v23
	v_mul_f32_e32 v22, v32, v70
	v_fmaak_f32 v16, v16, v22, 0xc1e6d4ca
	v_mul_f32_e32 v22, v33, v70
	v_fmaak_f32 v17, v17, v22, 0xc1e6d4ca
	v_mul_f32_e32 v22, v34, v70
	v_fmaak_f32 v18, v18, v22, 0xc1e6d4ca
	v_mul_f32_e32 v22, v35, v70
	v_fmaak_f32 v19, v19, v22, 0xc1e6d4ca
	v_exp_f32_e32 v20, v20
	v_exp_f32_e32 v16, v16
	v_exp_f32_e32 v18, v18
	v_exp_f32_e32 v19, v19
	v_exp_f32_e32 v22, v17
	v_cvt_pk_bf16_f32 v28, v28, v36
	v_cvt_pk_bf16_f32 v20, v20, v24
	v_cvt_pk_bf16_f32 v17, v18, v19
	v_cvt_pk_bf16_f32 v16, v16, v22
	ds_write_b64 v60, v[28:29] offset:10304
	ds_write_b64 v53, v[20:21] offset:10304
	ds_write_b64 v48, v[16:17] offset:10304
	ds_read_b128 v[16:19], v71 offset:9024
	v_mov_b32_e32 v20, 0xc1e6d4ca
	s_waitcnt lgkmcnt(0)
	v_mul_f32_e32 v21, v16, v64
	v_fmaak_f32 v12, v12, v21, 0xc1e6d4ca
	v_mul_f32_e32 v21, v18, v64
	v_fmaak_f32 v14, v14, v21, 0xc1e6d4ca
	v_mul_f32_e32 v21, v19, v64
	v_fmaak_f32 v15, v15, v21, 0xc1e6d4ca
	v_exp_f32_e32 v14, v14
	v_exp_f32_e32 v15, v15
	v_mul_f32_e32 v21, v17, v64
	v_fmaak_f32 v13, v13, v21, 0xc1e6d4ca
	v_exp_f32_e32 v21, v13
	v_cvt_pk_bf16_f32 v13, v14, v15
	v_mul_f32_e32 v14, v16, v65
	v_fmaak_f32 v8, v8, v14, 0xc1e6d4ca
	v_mul_f32_e32 v14, v17, v65
	v_fmaak_f32 v9, v9, v14, 0xc1e6d4ca
	v_mul_f32_e32 v14, v18, v65
	v_fmaak_f32 v10, v10, v14, 0xc1e6d4ca
	v_mul_f32_e32 v14, v19, v65
	v_fmaak_f32 v11, v11, v14, 0xc1e6d4ca
	v_exp_f32_e32 v8, v8
	v_exp_f32_e32 v10, v10
	v_exp_f32_e32 v11, v11
	v_exp_f32_e32 v14, v9
	v_exp_f32_e32 v12, v12
	v_and_b32_e32 v64, 1, v100
	v_cvt_pk_bf16_f32 v9, v10, v11
	v_cvt_pk_bf16_f32 v8, v8, v14
	ds_write_b64 v58, v[8:9] offset:10336
	v_mul_f32_e32 v8, v16, v68
	v_fmaak_f32 v4, v4, v8, 0xc1e6d4ca
	v_mul_f32_e32 v8, v18, v68
	v_fmaak_f32 v6, v6, v8, 0xc1e6d4ca
	v_mul_f32_e32 v8, v19, v68
	v_fmaak_f32 v7, v7, v8, 0xc1e6d4ca
	v_exp_f32_e32 v6, v6
	v_exp_f32_e32 v7, v7
	v_mul_f32_e32 v8, v17, v68
	v_fmaak_f32 v5, v5, v8, 0xc1e6d4ca
	v_exp_f32_e32 v8, v5
	v_cvt_pk_bf16_f32 v5, v6, v7
	v_mul_f32_e32 v6, v16, v70
	v_fmaak_f32 v0, v0, v6, 0xc1e6d4ca
	v_mul_f32_e32 v6, v17, v70
	v_fmaak_f32 v1, v1, v6, 0xc1e6d4ca
	v_mul_f32_e32 v6, v18, v70
	v_fmaak_f32 v2, v2, v6, 0xc1e6d4ca
	v_mul_f32_e32 v6, v19, v70
	v_fmac_f32_e32 v20, v3, v6
	v_exp_f32_e32 v0, v0
	v_exp_f32_e32 v2, v2
	v_exp_f32_e32 v3, v20
	v_exp_f32_e32 v6, v1
	v_exp_f32_e32 v4, v4
	v_cvt_pk_bf16_f32 v12, v12, v21
	v_cvt_pk_bf16_f32 v1, v2, v3
	v_cvt_pk_bf16_f32 v0, v0, v6
	ds_write_b64 v48, v[0:1] offset:10336
	v_lshrrev_b32_e32 v0, 2, v101
	v_or_b32_e32 v0, v67, v0
	v_lshlrev_b32_e32 v1, 3, v100
	v_mul_u32_u24_e32 v0, 0x88, v0
	v_and_b32_e32 v1, 24, v1
	v_add_u32_e32 v2, s6, v66
	v_cvt_pk_bf16_f32 v4, v4, v8
	v_add3_u32 v62, s6, v0, v1
	v_mad_u32_u24 v0, v101, s2, v2
	ds_write_b64 v60, v[12:13] offset:10336
	ds_write_b64 v53, v[4:5] offset:10336
	v_add_u32_e32 v1, 0x2800, v0
	v_add_u32_e32 v0, 0x2840, v0
	ds_read2_b64 v[24:27], v1 offset1:1
	ds_read2_b64 v[28:31], v0 offset1:1
	ds_read_b64_tr_b16 v[34:35], v62 offset:10784
	ds_read_b64_tr_b16 v[36:37], v62 offset:14592
	ds_read_b64_tr_b16 v[38:39], v62 offset:15136
	ds_read_b64_tr_b16 v[32:33], v62 offset:10240
	ds_read_b64_tr_b16 v[40:41], v62 offset:10272
	v_add_u32_e32 v0, v2, v57
	v_cndmask_b32_e64 v68, 0, -1, s[0:1]
	s_mov_b32 s0, 0x3f803f80
	v_add_u32_e32 v1, 0x2800, v0
	v_add_u32_e32 v0, 0x2840, v0
	s_mov_b32 s2, s0
	s_mov_b32 s3, s0
	ds_read2_b64 v[16:19], v1 offset1:1
	ds_read2_b64 v[20:23], v0 offset1:1
	ds_read_b64_tr_b16 v[42:43], v62 offset:10816
	ds_read_b64_tr_b16 v[44:45], v62 offset:14624
	ds_read_b64_tr_b16 v[46:47], v62 offset:15168
	v_add_u32_e32 v0, v2, v52
	s_mov_b32 s1, s0
	v_mov_b64_e32 v[78:79], s[2:3]
	v_add_u32_e32 v1, 0x2800, v0
	v_add_u32_e32 v0, 0x2840, v0
	v_add_u32_e32 v4, v2, v56
	v_mov_b64_e32 v[76:77], s[0:1]
	ds_read2_b64 v[8:11], v1 offset1:1
	ds_read2_b64 v[12:15], v0 offset1:1
	ds_read_b64_tr_b16 v[48:49], v62 offset:10304
	ds_read_b64_tr_b16 v[50:51], v62 offset:10848
	ds_read_b64_tr_b16 v[52:53], v62 offset:14656
	ds_read_b64_tr_b16 v[54:55], v62 offset:15200
	v_add_u32_e32 v0, 0x2800, v4
	v_cmp_eq_u32_e32 vcc, 0, v64
	v_mov_b32_e32 v65, 0xeeeeeeee
	v_mov_b32_e32 v67, 0x44444444
	ds_read2_b64 v[0:3], v0 offset1:1
	v_cndmask_b32_e32 v72, v65, v67, vcc
	v_lshlrev_b32_e32 v65, 1, v66
	v_lshlrev_b32_e32 v64, 2, v64
	v_add3_u32 v96, s8, v65, v64
	s_mov_b32 s8, 0x2b8cbccc
	v_mov_b64_e32 v[82:83], s[10:11]
	v_mov_b64_e32 v[80:81], s[8:9]
	v_mov_b64_e32 v[86:87], s[10:11]
	v_mov_b64_e32 v[84:85], s[8:9]
	s_waitcnt lgkmcnt(14)
	v_smfmac_f32_16x16x64_bf16 v[80:83], v[76:79], v[24:31], v72
	v_mov_b64_e32 v[90:91], s[10:11]
	v_mov_b64_e32 v[94:95], s[10:11]
	v_add_u32_e32 v4, 0x2840, v4
	v_cmp_eq_u32_e32 vcc, 1, v75
	s_waitcnt lgkmcnt(10)
	v_smfmac_f32_16x16x64_bf16 v[84:87], v[76:79], v[16:23], v72
	v_mov_b64_e32 v[88:89], s[8:9]
	v_mov_b64_e32 v[92:93], s[8:9]
	ds_read2_b64 v[4:7], v4 offset1:1
	ds_read_b64_tr_b16 v[56:57], v62 offset:10336
	ds_read_b64_tr_b16 v[58:59], v62 offset:10880
	ds_read_b64_tr_b16 v[60:61], v62 offset:14688
	ds_read_b64_tr_b16 v[62:63], v62 offset:15232
	ds_read2st64_b32 v[70:71], v102 offset0:22 offset1:23
	v_cndmask_b32_e64 v73, 0, -1, vcc
	v_cmp_eq_u32_e32 vcc, 2, v75
	s_waitcnt lgkmcnt(11)
	v_smfmac_f32_16x16x64_bf16 v[88:91], v[76:79], v[8:15], v72
	v_mov_b64_e32 v[66:67], s[10:11]
	v_cndmask_b32_e64 v74, 0, -1, vcc
	v_cmp_eq_u32_e32 vcc, 3, v75
	s_waitcnt lgkmcnt(5)
	v_smfmac_f32_16x16x64_bf16 v[92:95], v[76:79], v[0:7], v72
	v_add_f32_e32 v77, v80, v81
	v_cndmask_b32_e64 v75, 0, -1, vcc
	v_add_f32_e32 v76, v84, v85
	v_and_b32_e32 v77, v68, v77
	v_and_or_b32 v76, v73, v76, v77
	v_add_f32_e32 v77, v88, v89
	s_nop 1
	v_add_f32_e32 v78, v92, v93
	v_and_b32_e32 v77, v74, v77
	v_and_b32_e32 v78, v75, v78
	v_or3_b32 v76, v76, v77, v78
	v_rcp_f32_e32 v77, v76
	v_lshlrev_b32_e32 v76, 1, v100
	v_sub_u32_e32 v76, v102, v76
	s_waitcnt lgkmcnt(0)
	v_mul_f32_e32 v77, v71, v77
	v_cvt_pk_bf16_f32 v77, v77, s0
	ds_write_b16 v76, v77 offset:6144
	v_add_u32_e32 v77, 0x1800, v96
	ds_read2_b32 v[78:79], v77 offset1:2
	ds_read2_b32 v[80:81], v77 offset0:4 offset1:6
	v_mov_b64_e32 v[84:85], s[10:11]
	v_mov_b64_e32 v[82:83], s[8:9]
	v_mov_b64_e32 v[88:89], s[10:11]
	v_mov_b64_e32 v[86:87], s[8:9]
	s_waitcnt lgkmcnt(0)
	v_smfmac_f32_16x16x64_bf16 v[82:85], v[78:81], v[32:39], v72
	v_mov_b64_e32 v[92:93], s[10:11]
	v_mov_b64_e32 v[96:97], s[10:11]
	v_mov_b64_e32 v[90:91], s[8:9]
	v_smfmac_f32_16x16x64_bf16 v[86:89], v[78:81], v[40:47], v72
	v_mov_b64_e32 v[94:95], s[8:9]
	v_mov_b64_e32 v[64:65], s[8:9]
	v_smfmac_f32_16x16x64_bf16 v[90:93], v[78:81], v[48:55], v72
	v_smfmac_f32_16x16x64_bf16 v[94:97], v[78:81], v[56:63], v72
	v_add_f32_e32 v78, v82, v83
	v_and_b32_e32 v78, v68, v78
	s_nop 1
	v_add_f32_e32 v79, v86, v87
	v_and_or_b32 v78, v73, v79, v78
	s_nop 0
	v_add_f32_e32 v79, v90, v91
	v_add_f32_e32 v80, v94, v95
	v_and_b32_e32 v79, v74, v79
	v_and_b32_e32 v80, v75, v80
	v_or3_b32 v78, v78, v79, v80
	v_rcp_f32_e32 v78, v78
	v_mov_b64_e32 v[84:85], s[10:11]
	v_mov_b64_e32 v[82:83], s[8:9]
	v_mul_f32_e32 v78, v70, v78
	v_cvt_pk_bf16_f32 v78, v78, s0
	ds_write_b16 v76, v78 offset:6144
	s_movk_i32 s30, 98
.Lsk_loop:
	ds_read2_b32 v[78:79], v77 offset1:2
	ds_read2_b32 v[80:81], v77 offset0:4 offset1:6
	v_mov_b64_e32 v[88:89], s[10:11]
	s_waitcnt lgkmcnt(0)
	v_smfmac_f32_16x16x64_bf16 v[82:85], v[78:81], v[24:31], v72
	v_mov_b64_e32 v[86:87], s[8:9]
	v_mov_b64_e32 v[92:93], s[10:11]
	v_mov_b64_e32 v[96:97], s[10:11]
	v_smfmac_f32_16x16x64_bf16 v[86:89], v[78:81], v[16:23], v72
	v_mov_b64_e32 v[90:91], s[8:9]
	v_mov_b64_e32 v[94:95], s[8:9]
	s_nop 0
	v_smfmac_f32_16x16x64_bf16 v[90:93], v[78:81], v[8:15], v72
	v_smfmac_f32_16x16x64_bf16 v[94:97], v[78:81], v[0:7], v72
	v_add_f32_e32 v79, v82, v83
	s_nop 1
	v_add_f32_e32 v78, v86, v87
	v_and_b32_e32 v79, v68, v79
	v_and_or_b32 v78, v73, v78, v79
	s_nop 0
	v_add_f32_e32 v79, v90, v91
	v_add_f32_e32 v80, v94, v95
	v_and_b32_e32 v79, v74, v79
	v_and_b32_e32 v80, v75, v80
	v_or3_b32 v78, v78, v79, v80
	v_rcp_f32_e32 v78, v78
	v_mov_b64_e32 v[84:85], s[10:11]
	v_mov_b64_e32 v[82:83], s[8:9]
	v_mul_f32_e32 v78, v71, v78
	v_cvt_pk_bf16_f32 v78, v78, s0
	ds_write_b16 v76, v78 offset:6144
	ds_read2_b32 v[78:79], v77 offset1:2
	ds_read2_b32 v[80:81], v77 offset0:4 offset1:6
	v_mov_b64_e32 v[88:89], s[10:11]
	s_waitcnt lgkmcnt(0)
	v_smfmac_f32_16x16x64_bf16 v[82:85], v[78:81], v[32:39], v72
	v_mov_b64_e32 v[86:87], s[8:9]
	v_mov_b64_e32 v[92:93], s[10:11]
	v_mov_b64_e32 v[96:97], s[10:11]
	v_smfmac_f32_16x16x64_bf16 v[86:89], v[78:81], v[40:47], v72
	v_mov_b64_e32 v[90:91], s[8:9]
	v_mov_b64_e32 v[94:95], s[8:9]
	s_nop 0
	v_smfmac_f32_16x16x64_bf16 v[90:93], v[78:81], v[48:55], v72
	v_smfmac_f32_16x16x64_bf16 v[94:97], v[78:81], v[56:63], v72
	v_add_f32_e32 v78, v82, v83
	v_and_b32_e32 v78, v68, v78
	s_nop 0
	v_add_f32_e32 v79, v86, v87
	v_and_or_b32 v78, v73, v79, v78
	s_nop 1
	v_add_f32_e32 v79, v90, v91
	v_add_f32_e32 v80, v94, v95
	v_and_b32_e32 v79, v74, v79
	v_and_b32_e32 v80, v75, v80
	v_or3_b32 v78, v78, v79, v80
	v_rcp_f32_e32 v78, v78
	v_mov_b64_e32 v[84:85], s[10:11]
	v_mov_b64_e32 v[82:83], s[8:9]
	v_mul_f32_e32 v78, v70, v78
	v_cvt_pk_bf16_f32 v78, v78, s0
	ds_write_b16 v76, v78 offset:6144
	s_add_i32 s30, s30, -1
	s_cmp_lg_u32 s30, 0
	s_cbranch_scc1 .Lsk_loop
	ds_read2_b32 v[78:79], v77 offset1:2
	ds_read2_b32 v[80:81], v77 offset0:4 offset1:6
	v_mov_b64_e32 v[88:89], s[10:11]
	s_waitcnt lgkmcnt(0)
	v_smfmac_f32_16x16x64_bf16 v[82:85], v[78:81], v[24:31], v72
	v_mov_b64_e32 v[86:87], s[8:9]
	v_mov_b64_e32 v[92:93], s[10:11]
	v_mov_b64_e32 v[96:97], s[10:11]
	v_smfmac_f32_16x16x64_bf16 v[86:89], v[78:81], v[16:23], v72
	v_mov_b64_e32 v[90:91], s[8:9]
	v_mov_b64_e32 v[94:95], s[8:9]
	s_nop 0
	v_smfmac_f32_16x16x64_bf16 v[90:93], v[78:81], v[8:15], v72
	v_smfmac_f32_16x16x64_bf16 v[94:97], v[78:81], v[0:7], v72
	v_add_f32_e32 v79, v82, v83
	s_nop 1
	v_add_f32_e32 v78, v86, v87
	v_and_b32_e32 v79, v68, v79
	v_and_or_b32 v78, v73, v78, v79
	s_nop 0
	v_add_f32_e32 v79, v90, v91
	v_add_f32_e32 v80, v94, v95
	v_and_b32_e32 v79, v74, v79
	v_and_b32_e32 v80, v75, v80
	v_or3_b32 v78, v78, v79, v80
	v_rcp_f32_e32 v78, v78
	v_mov_b64_e32 v[84:85], s[10:11]
	v_mov_b64_e32 v[82:83], s[8:9]
	v_mul_f32_e32 v78, v71, v78
	v_cvt_pk_bf16_f32 v78, v78, s0
	ds_write_b16 v76, v78 offset:6144
	ds_read2_b32 v[78:79], v77 offset1:2
	ds_read2_b32 v[80:81], v77 offset0:4 offset1:6
	s_waitcnt lgkmcnt(0)
	v_smfmac_f32_16x16x64_bf16 v[82:85], v[78:81], v[32:39], v72
	v_mov_b64_e32 v[34:35], s[10:11]
	v_mov_b64_e32 v[32:33], s[8:9]
	v_mov_b64_e32 v[38:39], s[10:11]
	v_mov_b64_e32 v[36:37], s[8:9]
	v_smfmac_f32_16x16x64_bf16 v[32:35], v[78:81], v[40:47], v72
	v_mov_b64_e32 v[42:43], s[10:11]
	v_mov_b64_e32 v[40:41], s[8:9]
	s_nop 0
	v_add_f32_e32 v44, v82, v83
	v_smfmac_f32_16x16x64_bf16 v[36:39], v[78:81], v[48:55], v72
	v_and_b32_e32 v44, v68, v44
	s_nop 1
	v_add_f32_e32 v45, v32, v33
	v_and_or_b32 v44, v73, v45, v44
	v_smfmac_f32_16x16x64_bf16 v[40:43], v[78:81], v[56:63], v72
	s_nop 1
	v_add_f32_e32 v45, v36, v37
	v_and_b32_e32 v45, v74, v45
	v_mov_b64_e32 v[38:39], s[10:11]
	s_nop 2
	v_add_f32_e32 v46, v40, v41
	v_and_b32_e32 v46, v75, v46
	v_or3_b32 v44, v44, v45, v46
	v_rcp_f32_e32 v44, v44
	v_mov_b64_e32 v[36:37], s[8:9]
	v_mov_b64_e32 v[42:43], s[10:11]
	v_mov_b64_e32 v[40:41], s[8:9]
	v_mul_f32_e32 v32, v70, v44
	v_cvt_pk_bf16_f32 v32, v32, s0
	ds_write_b16 v76, v32 offset:6144
	ds_read2_b32 v[48:49], v77 offset1:2
	ds_read2_b32 v[50:51], v77 offset0:4 offset1:6
	v_mov_b64_e32 v[34:35], s[10:11]
	v_mov_b64_e32 v[32:33], s[8:9]
	v_mov_b64_e32 v[46:47], s[10:11]
	s_waitcnt lgkmcnt(0)
	v_smfmac_f32_16x16x64_bf16 v[36:39], v[48:51], v[16:23], v72
	v_mov_b64_e32 v[44:45], s[8:9]
	v_and_b32_e32 v55, 0xffff0000, v24
	v_log_f32_e32 v57, v55
	v_smfmac_f32_16x16x64_bf16 v[32:35], v[48:51], v[24:31], v72
	s_nop 3
	v_add_f32_e32 v52, v36, v37
	s_mov_b32 s0, 0x3d0df4e0
	v_and_b32_e32 v59, 0xffff0000, v26
	v_smfmac_f32_16x16x64_bf16 v[40:43], v[48:51], v[8:15], v72
	v_lshlrev_b32_e32 v58, 16, v26
	v_add_f32_e32 v53, v32, v33
	v_and_b32_e32 v53, v68, v53
	v_smfmac_f32_16x16x64_bf16 v[44:47], v[48:51], v[0:7], v72
	v_and_or_b32 v52, v73, v52, v53
	s_nop 2
	v_add_f32_e32 v53, v40, v41
	v_and_b32_e32 v53, v74, v53
	v_log_f32_e32 v60, v58
	v_log_f32_e32 v61, v59
	v_add_f32_e32 v54, v44, v45
	v_and_b32_e32 v54, v75, v54
	v_or3_b32 v52, v52, v53, v54
	v_lshlrev_b32_e32 v54, 16, v24
	v_log_f32_e32 v56, v54
	v_rcp_f32_e32 v52, v52
	v_pk_fma_f32 v[56:57], v[56:57], s[0:1], 1.0 op_sel_hi:[1,0,0]
	v_mul_f32_e32 v52, v71, v52
	v_pk_mul_f32 v[54:55], v[56:57], v[54:55]
	s_nop 0
	v_cvt_pk_bf16_f32 v24, v54, v55
	v_and_b32_e32 v55, 0xffff0000, v25
	v_lshlrev_b32_e32 v54, 16, v25
	v_log_f32_e32 v56, v54
	v_log_f32_e32 v57, v55
	s_nop 0
	v_pk_fma_f32 v[56:57], v[56:57], s[0:1], 1.0 op_sel_hi:[1,0,0]
	s_nop 0
	v_pk_mul_f32 v[54:55], v[56:57], v[54:55]
	s_nop 0
	v_cvt_pk_bf16_f32 v25, v54, v55
	v_pk_fma_f32 v[54:55], v[60:61], s[0:1], 1.0 op_sel_hi:[1,0,0]
	s_nop 0
	v_pk_mul_f32 v[54:55], v[54:55], v[58:59]
	v_and_b32_e32 v59, 0xffff0000, v28
	v_cvt_pk_bf16_f32 v26, v54, v55
	v_and_b32_e32 v55, 0xffff0000, v27
	v_lshlrev_b32_e32 v54, 16, v27
	v_log_f32_e32 v56, v54
	v_log_f32_e32 v57, v55
	v_lshlrev_b32_e32 v58, 16, v28
	v_log_f32_e32 v60, v58
	v_log_f32_e32 v61, v59
	v_pk_fma_f32 v[56:57], v[56:57], s[0:1], 1.0 op_sel_hi:[1,0,0]
	s_nop 0
	v_pk_mul_f32 v[54:55], v[56:57], v[54:55]
	s_nop 0
	v_cvt_pk_bf16_f32 v27, v54, v55
	v_pk_fma_f32 v[54:55], v[60:61], s[0:1], 1.0 op_sel_hi:[1,0,0]
	s_nop 0
	v_pk_mul_f32 v[54:55], v[54:55], v[58:59]
	v_and_b32_e32 v59, 0xffff0000, v30
	v_cvt_pk_bf16_f32 v28, v54, v55
	v_and_b32_e32 v55, 0xffff0000, v29
	v_lshlrev_b32_e32 v54, 16, v29
	v_log_f32_e32 v56, v54
	v_log_f32_e32 v57, v55
	v_lshlrev_b32_e32 v58, 16, v30
	v_log_f32_e32 v60, v58
	v_log_f32_e32 v61, v59
	v_pk_fma_f32 v[56:57], v[56:57], s[0:1], 1.0 op_sel_hi:[1,0,0]
	s_nop 0
	v_pk_mul_f32 v[54:55], v[56:57], v[54:55]
	s_nop 0
	v_cvt_pk_bf16_f32 v29, v54, v55
	v_pk_fma_f32 v[54:55], v[60:61], s[0:1], 1.0 op_sel_hi:[1,0,0]
	s_nop 0
	v_pk_mul_f32 v[54:55], v[54:55], v[58:59]
	v_and_b32_e32 v59, 0xffff0000, v16
	v_cvt_pk_bf16_f32 v30, v54, v55
	v_and_b32_e32 v55, 0xffff0000, v31
	v_lshlrev_b32_e32 v54, 16, v31
	v_log_f32_e32 v56, v54
	v_log_f32_e32 v57, v55
	v_lshlrev_b32_e32 v58, 16, v16
	v_log_f32_e32 v60, v58
	v_log_f32_e32 v61, v59
	v_pk_fma_f32 v[56:57], v[56:57], s[0:1], 1.0 op_sel_hi:[1,0,0]
	s_nop 0
	v_pk_mul_f32 v[54:55], v[56:57], v[54:55]
	s_nop 0
	v_cvt_pk_bf16_f32 v31, v54, v55
	v_pk_fma_f32 v[54:55], v[60:61], s[0:1], 1.0 op_sel_hi:[1,0,0]
	s_nop 0
	v_pk_mul_f32 v[54:55], v[54:55], v[58:59]
	v_and_b32_e32 v59, 0xffff0000, v18
	v_cvt_pk_bf16_f32 v16, v54, v55
	v_and_b32_e32 v55, 0xffff0000, v17
	v_lshlrev_b32_e32 v54, 16, v17
	v_log_f32_e32 v56, v54
	v_log_f32_e32 v57, v55
	v_lshlrev_b32_e32 v58, 16, v18
	v_log_f32_e32 v60, v58
	v_log_f32_e32 v61, v59
	v_pk_fma_f32 v[56:57], v[56:57], s[0:1], 1.0 op_sel_hi:[1,0,0]
	s_nop 0
	v_pk_mul_f32 v[54:55], v[56:57], v[54:55]
	s_nop 0
	v_cvt_pk_bf16_f32 v17, v54, v55
	v_pk_fma_f32 v[54:55], v[60:61], s[0:1], 1.0 op_sel_hi:[1,0,0]
	s_nop 0
	v_pk_mul_f32 v[54:55], v[54:55], v[58:59]
	v_and_b32_e32 v59, 0xffff0000, v20
	v_cvt_pk_bf16_f32 v18, v54, v55
	v_and_b32_e32 v55, 0xffff0000, v19
	v_lshlrev_b32_e32 v54, 16, v19
	v_log_f32_e32 v56, v54
	v_log_f32_e32 v57, v55
	v_lshlrev_b32_e32 v58, 16, v20
	v_log_f32_e32 v60, v58
	v_log_f32_e32 v61, v59
	v_pk_fma_f32 v[56:57], v[56:57], s[0:1], 1.0 op_sel_hi:[1,0,0]
	s_nop 0
	v_pk_mul_f32 v[54:55], v[56:57], v[54:55]
	s_nop 0
	v_cvt_pk_bf16_f32 v19, v54, v55
	v_pk_fma_f32 v[54:55], v[60:61], s[0:1], 1.0 op_sel_hi:[1,0,0]
	s_nop 0
	v_pk_mul_f32 v[54:55], v[54:55], v[58:59]
	v_and_b32_e32 v59, 0xffff0000, v22
	v_cvt_pk_bf16_f32 v20, v54, v55
	v_and_b32_e32 v55, 0xffff0000, v21
	v_lshlrev_b32_e32 v54, 16, v21
	v_log_f32_e32 v56, v54
	v_log_f32_e32 v57, v55
	v_lshlrev_b32_e32 v58, 16, v22
	v_log_f32_e32 v60, v58
	v_log_f32_e32 v61, v59
	v_pk_fma_f32 v[56:57], v[56:57], s[0:1], 1.0 op_sel_hi:[1,0,0]
	s_nop 0
	v_pk_mul_f32 v[54:55], v[56:57], v[54:55]
	s_nop 0
	v_cvt_pk_bf16_f32 v21, v54, v55
	v_pk_fma_f32 v[54:55], v[60:61], s[0:1], 1.0 op_sel_hi:[1,0,0]
	s_nop 0
	v_pk_mul_f32 v[54:55], v[54:55], v[58:59]
	v_and_b32_e32 v59, 0xffff0000, v8
	v_cvt_pk_bf16_f32 v22, v54, v55
	v_and_b32_e32 v55, 0xffff0000, v23
	v_lshlrev_b32_e32 v54, 16, v23
	v_log_f32_e32 v56, v54
	v_log_f32_e32 v57, v55
	v_lshlrev_b32_e32 v58, 16, v8
	v_log_f32_e32 v60, v58
	v_log_f32_e32 v61, v59
	v_pk_fma_f32 v[56:57], v[56:57], s[0:1], 1.0 op_sel_hi:[1,0,0]
	s_nop 0
	v_pk_mul_f32 v[54:55], v[56:57], v[54:55]
	s_nop 0
	v_cvt_pk_bf16_f32 v23, v54, v55
	v_pk_fma_f32 v[54:55], v[60:61], s[0:1], 1.0 op_sel_hi:[1,0,0]
	s_nop 0
	v_pk_mul_f32 v[54:55], v[54:55], v[58:59]
	v_and_b32_e32 v59, 0xffff0000, v10
	v_cvt_pk_bf16_f32 v8, v54, v55
	v_and_b32_e32 v55, 0xffff0000, v9
	v_lshlrev_b32_e32 v54, 16, v9
	v_log_f32_e32 v56, v54
	v_log_f32_e32 v57, v55
	v_lshlrev_b32_e32 v58, 16, v10
	v_log_f32_e32 v60, v58
	v_log_f32_e32 v61, v59
	v_pk_fma_f32 v[56:57], v[56:57], s[0:1], 1.0 op_sel_hi:[1,0,0]
	s_nop 0
	v_pk_mul_f32 v[54:55], v[56:57], v[54:55]
	s_nop 0
	v_cvt_pk_bf16_f32 v9, v54, v55
	v_pk_fma_f32 v[54:55], v[60:61], s[0:1], 1.0 op_sel_hi:[1,0,0]
	s_nop 0
	v_pk_mul_f32 v[54:55], v[54:55], v[58:59]
	v_and_b32_e32 v59, 0xffff0000, v12
	v_cvt_pk_bf16_f32 v10, v54, v55
	v_and_b32_e32 v55, 0xffff0000, v11
	v_lshlrev_b32_e32 v54, 16, v11
	v_log_f32_e32 v56, v54
	v_log_f32_e32 v57, v55
	v_lshlrev_b32_e32 v58, 16, v12
	v_log_f32_e32 v60, v58
	v_log_f32_e32 v61, v59
	v_pk_fma_f32 v[56:57], v[56:57], s[0:1], 1.0 op_sel_hi:[1,0,0]
	s_nop 0
	v_pk_mul_f32 v[54:55], v[56:57], v[54:55]
	s_nop 0
	v_cvt_pk_bf16_f32 v11, v54, v55
	v_pk_fma_f32 v[54:55], v[60:61], s[0:1], 1.0 op_sel_hi:[1,0,0]
	s_nop 0
	v_pk_mul_f32 v[54:55], v[54:55], v[58:59]
	v_and_b32_e32 v59, 0xffff0000, v14
	v_cvt_pk_bf16_f32 v12, v54, v55
	v_and_b32_e32 v55, 0xffff0000, v13
	v_lshlrev_b32_e32 v54, 16, v13
	v_log_f32_e32 v56, v54
	v_log_f32_e32 v57, v55
	v_lshlrev_b32_e32 v58, 16, v14
	v_log_f32_e32 v60, v58
	v_log_f32_e32 v61, v59
	v_pk_fma_f32 v[56:57], v[56:57], s[0:1], 1.0 op_sel_hi:[1,0,0]
	s_nop 0
	v_pk_mul_f32 v[54:55], v[56:57], v[54:55]
	s_nop 0
	v_cvt_pk_bf16_f32 v13, v54, v55
	v_pk_fma_f32 v[54:55], v[60:61], s[0:1], 1.0 op_sel_hi:[1,0,0]
	s_nop 0
	v_pk_mul_f32 v[54:55], v[54:55], v[58:59]
	v_and_b32_e32 v59, 0xffff0000, v0
	v_cvt_pk_bf16_f32 v14, v54, v55
	v_and_b32_e32 v55, 0xffff0000, v15
	v_lshlrev_b32_e32 v54, 16, v15
	v_log_f32_e32 v56, v54
	v_log_f32_e32 v57, v55
	v_lshlrev_b32_e32 v58, 16, v0
	v_log_f32_e32 v60, v58
	v_log_f32_e32 v61, v59
	v_pk_fma_f32 v[56:57], v[56:57], s[0:1], 1.0 op_sel_hi:[1,0,0]
	s_nop 0
	v_pk_mul_f32 v[54:55], v[56:57], v[54:55]
	s_nop 0
	v_cvt_pk_bf16_f32 v15, v54, v55
	v_pk_fma_f32 v[54:55], v[60:61], s[0:1], 1.0 op_sel_hi:[1,0,0]
	s_nop 0
	v_pk_mul_f32 v[54:55], v[54:55], v[58:59]
	v_and_b32_e32 v59, 0xffff0000, v2
	v_cvt_pk_bf16_f32 v0, v54, v55
	v_and_b32_e32 v55, 0xffff0000, v1
	v_lshlrev_b32_e32 v54, 16, v1
	v_log_f32_e32 v56, v54
	v_log_f32_e32 v57, v55
	v_lshlrev_b32_e32 v58, 16, v2
	v_log_f32_e32 v60, v58
	v_log_f32_e32 v61, v59
	v_pk_fma_f32 v[56:57], v[56:57], s[0:1], 1.0 op_sel_hi:[1,0,0]
	s_nop 0
	v_pk_mul_f32 v[54:55], v[56:57], v[54:55]
	s_nop 0
	v_cvt_pk_bf16_f32 v1, v54, v55
	v_pk_fma_f32 v[54:55], v[60:61], s[0:1], 1.0 op_sel_hi:[1,0,0]
	s_nop 0
	v_pk_mul_f32 v[54:55], v[54:55], v[58:59]
	v_and_b32_e32 v59, 0xffff0000, v4
	v_cvt_pk_bf16_f32 v2, v54, v55
	v_and_b32_e32 v55, 0xffff0000, v3
	v_lshlrev_b32_e32 v54, 16, v3
	v_log_f32_e32 v56, v54
	v_log_f32_e32 v57, v55
	v_lshlrev_b32_e32 v58, 16, v4
	v_log_f32_e32 v60, v58
	v_log_f32_e32 v61, v59
	v_pk_fma_f32 v[56:57], v[56:57], s[0:1], 1.0 op_sel_hi:[1,0,0]
	s_nop 0
	v_pk_mul_f32 v[54:55], v[56:57], v[54:55]
	s_nop 0
	v_cvt_pk_bf16_f32 v3, v54, v55
	v_pk_fma_f32 v[54:55], v[60:61], s[0:1], 1.0 op_sel_hi:[1,0,0]
	s_nop 0
	v_pk_mul_f32 v[54:55], v[54:55], v[58:59]
	v_and_b32_e32 v59, 0xffff0000, v6
	v_cvt_pk_bf16_f32 v4, v54, v55
	v_and_b32_e32 v55, 0xffff0000, v5
	v_lshlrev_b32_e32 v54, 16, v5
	v_log_f32_e32 v56, v54
	v_log_f32_e32 v57, v55
	v_lshlrev_b32_e32 v58, 16, v6
	v_log_f32_e32 v60, v58
	v_log_f32_e32 v61, v59
	v_pk_fma_f32 v[56:57], v[56:57], s[0:1], 1.0 op_sel_hi:[1,0,0]
	s_nop 0
	v_pk_mul_f32 v[54:55], v[56:57], v[54:55]
	s_nop 0
	v_cvt_pk_bf16_f32 v5, v54, v55
	v_pk_fma_f32 v[54:55], v[60:61], s[0:1], 1.0 op_sel_hi:[1,0,0]
	v_and_b32_e32 v61, 0xffff0000, v7
	v_pk_mul_f32 v[58:59], v[54:55], v[58:59]
	v_mov_b64_e32 v[56:57], s[10:11]
	v_mov_b64_e32 v[54:55], s[8:9]
	v_lshlrev_b32_e32 v60, 16, v7
	v_cvt_pk_bf16_f32 v6, v58, v59
	v_smfmac_f32_16x16x64_bf16 v[54:57], v[48:51], v[24:31], v72
	v_log_f32_e32 v28, v60
	v_mov_b64_e32 v[26:27], s[10:11]
	v_log_f32_e32 v29, v61
	v_mov_b64_e32 v[24:25], s[8:9]
	s_nop 1
	v_smfmac_f32_16x16x64_bf16 v[24:27], v[48:51], v[16:23], v72
	v_mov_b64_e32 v[18:19], s[10:11]
	v_mov_b64_e32 v[16:17], s[8:9]
	s_nop 1
	v_smfmac_f32_16x16x64_bf16 v[16:19], v[48:51], v[8:15], v72
	v_fma_f32 v8, v28, s0, 1.0
	v_fma_f32 v9, v29, s0, 1.0
	v_pk_mul_f32 v[8:9], v[8:9], v[60:61]
	s_nop 0
	v_cvt_pk_bf16_f32 v7, v8, v9
	s_nop 1
	v_smfmac_f32_16x16x64_bf16 v[64:67], v[48:51], v[0:7], v72
	v_add_f32_e32 v0, v54, v55
	v_and_b32_e32 v0, v68, v0
	v_add_f32_e32 v1, v24, v25
	v_and_or_b32 v0, v73, v1, v0
	v_add_f32_e32 v1, v16, v17
	s_nop 2
	v_add_f32_e32 v2, v64, v65
	v_and_b32_e32 v1, v74, v1
	v_and_b32_e32 v2, v75, v2
	v_or3_b32 v0, v0, v1, v2
	v_and_b32_e32 v2, 64, v100
	v_add_u32_e32 v2, 64, v2
	v_xor_b32_e32 v3, 1, v100
	v_cmp_lt_i32_e32 vcc, v3, v2
	v_add_f32_e32 v0, 0xab8cbccc, v0
	v_mul_f32_e32 v1, v52, v0
	v_cndmask_b32_e32 v3, v100, v3, vcc
	v_lshlrev_b32_e32 v3, 2, v3
	ds_bpermute_b32 v1, v3, v1
	s_waitcnt lgkmcnt(0)
	v_fmac_f32_e32 v1, v52, v0
	v_xor_b32_e32 v0, 2, v100
	v_cmp_lt_i32_e32 vcc, v0, v2
	s_nop 1
	v_cndmask_b32_e32 v0, v100, v0, vcc
	v_lshlrev_b32_e32 v0, 2, v0
	ds_bpermute_b32 v0, v0, v1
	s_waitcnt lgkmcnt(0)
	v_add_f32_e32 v0, v1, v0
	v_xor_b32_e32 v1, 4, v100
	v_cmp_lt_i32_e32 vcc, v1, v2
	s_nop 1
	v_cndmask_b32_e32 v1, v100, v1, vcc
	v_lshlrev_b32_e32 v1, 2, v1
	ds_bpermute_b32 v1, v1, v0
	s_waitcnt lgkmcnt(0)
	v_add_f32_e32 v0, v0, v1
	v_xor_b32_e32 v1, 8, v100
	v_cmp_lt_i32_e32 vcc, v1, v2
	s_nop 1
	v_cndmask_b32_e32 v1, v100, v1, vcc
	v_lshlrev_b32_e32 v1, 2, v1
	ds_bpermute_b32 v1, v1, v0
	s_waitcnt lgkmcnt(0)
	v_add_f32_e32 v0, v0, v1
	v_xor_b32_e32 v1, 16, v100
	v_cmp_lt_i32_e32 vcc, v1, v2
	s_nop 1
	v_cndmask_b32_e32 v1, v100, v1, vcc
	v_lshlrev_b32_e32 v1, 2, v1
	ds_bpermute_b32 v1, v1, v0
	s_waitcnt lgkmcnt(0)
	v_add_f32_e32 v0, v0, v1
	v_xor_b32_e32 v1, 32, v100
	v_cmp_lt_i32_e32 vcc, v1, v2
	s_nop 1
	v_cndmask_b32_e32 v1, v100, v1, vcc
	v_lshlrev_b32_e32 v1, 2, v1
	ds_bpermute_b32 v1, v1, v0
	v_cmp_eq_u32_e32 vcc, 0, v100
	s_and_saveexec_b64 s[0:1], vcc
	s_cbranch_execz .LBB1_38
	s_mul_i32 s0, s22, 5
	s_add_i32 s0, s0, s23
	s_mov_b32 s1, 0
	s_lshl_b64 s[0:1], s[0:1], 2
	s_add_u32 s0, s12, s0
	s_waitcnt lgkmcnt(0)
	v_add_f32_e32 v0, v0, v1
	s_addc_u32 s1, s13, s1
	global_store_dword v69, v0, s[0:1]
